# k33: k26 + P6->P7 and P7->P8 grid barriers made XCD-local (leader skips release write-back and cross-XCD counter) when a run-time check finds blockIdx%8 == XCC id for every workgroup; falls back to th
# speedup vs baseline: 1.0053x; 1.0053x over previous
; __device__ __forceinline__ float sigmoidf_(float x) { return __builtin_amdgcn_rcpf(1.0f + __builtin_amdgcn_exp2f(-1.44269504089f * x)); }
; #define LAS __attribute__((address_space(3)))
; #define PROBE_BEGIN(k) do { if (PROBE_PH == (k)) { __syncthreads(); pr_t0 = __builtin_amdgcn_s_memrealtime(); } } while (0)
; __global__ void __launch_bounds__(NWAVES * 64, 2) fwd_kernel(Args args) {
;     ...
;     for (int u = tid; u < (LDS_BYTES - LDSCTL_OFF) / 4; u += NWAVES * 64) ((LAS unsigned*)(lds + LDSCTL_OFF))[u] = 0u;
;     __syncthreads();
;     XcdBarrier bar; bar.bar = (unsigned*)(ctl + CW_BAR); bar.x = 0; bar.st = nullptr;
;     if (N_LAUNCHES == 1) bar = xcd_barrier_post((unsigned*)(ctl + CW_BAR), MISC + 8);
;     ...
;     if (IN(0)) for (int rep_ = 0; rep_ < REP(0); ++rep_) {
;         PH_PTRS(); PROBE_BEGIN(0);
;         LAS float* CA = (LAS float*)(lds + RING_OFF);
;         LAS float* RED = (LAS float*)(lds + RING_OFF + 32768);
;         { f32x4 cv[4];
; #pragma unroll
;           for (int j = 0; j < 4; ++j) cv[j] = *(const f32x4*)(cin + 4 * (tid + 512 * j));
; #pragma unroll
;           for (int j = 0; j < 4; ++j) { f32x4 o; o[0] = cv[j][0] * sigmoidf_(cv[j][0]); o[1] = cv[j][1] * sigmoidf_(cv[j][1]); o[2] = cv[j][2] * sigmoidf_(cv[j][2]); o[3] = cv[j][3] * sigmoidf_(cv[j][3]); *(LAS f32x4*)(CA + 4 * (tid + 512 * j)) = o; } }
;         __syncthreads();
;         for (int it = vcu; it < 256; it += G) {
;             const int cb = it & 63, kq = it >> 6, col0 = cb * 256; const float* W; int N, cc;
;             if (col0 < 6 * D) { W = ada_w; N = 6 * D; cc = col0; } else { W = fada_w; N = 2 * D; cc = col0 - 6 * D; }
;             const int k0 = 512 * kq + 64 * wave;
;             f32x4 a0 = {0.f, 0.f, 0.f, 0.f}, a1 = a0, a2 = a0, a3 = a0;
;             const float* rowp = W + (size_t)__builtin_amdgcn_readfirstlane(k0) * N + cc; const unsigned voff = 16u * lane;
.LBB0_2:
	v_lshl_add_u32 v1, v0, 2, 0
	v_add_u32_e32 v1, 0x20000, v1
	v_mov_b32_e32 v2, 0
	ds_write2st64_b32 v1, v2, v2 offset1:8
	ds_write2st64_b32 v1, v2, v2 offset0:16 offset1:24
	v_or_b32_e32 v1, 0x800, v0
	s_mov_b64 s[4:5], -1
	s_and_saveexec_b64 s[6:7], s[4:5]
	v_lshl_add_u32 v3, v1, 2, 0
	v_add_u32_e32 v3, 0x20000, v3
	ds_write_b32 v3, v2
	s_or_b64 exec, exec, s[6:7]
	s_and_saveexec_b64 s[6:7], s[4:5]
	s_add_i32 s0, 0, 0x20000
	v_lshl_add_u32 v1, v1, 2, s0
	v_mov_b32_e32 v2, 0
	ds_write_b32 v1, v2 offset:2048
	s_or_b64 exec, exec, s[6:7]
	v_readlane_b32 s0, v254, 1
	v_readlane_b32 s1, v254, 2
	s_load_dwordx2 s[0:1], s[0:1], 0xf8
	v_or_b32_e32 v1, 0xc00, v0
	v_cmp_gt_u32_e64 s[4:5], 7, 6
	s_waitcnt lgkmcnt(0)
	v_writelane_b32 v254, s0, 5
	s_nop 1
	v_writelane_b32 v254, s1, 6
	v_cmp_gt_u32_e64 s[0:1], 7, 5
	s_and_saveexec_b64 s[6:7], s[0:1]
	v_lshl_add_u32 v2, v1, 2, 0
	v_add_u32_e32 v2, 0x20000, v2
	v_mov_b32_e32 v3, 0
	ds_write_b32 v2, v3
	s_or_b64 exec, exec, s[6:7]
	v_readlane_b32 s0, v254, 1
	v_readlane_b32 s1, v254, 2
	s_load_dwordx2 s[94:95], s[0:1], 0x100
	s_and_saveexec_b64 s[6:7], s[4:5]
	s_add_i32 s3, 0, 0x20000
	v_lshl_add_u32 v1, v1, 2, s3
	v_mov_b32_e32 v2, 0
	ds_write_b32 v1, v2 offset:2048
	s_or_b64 exec, exec, s[6:7]
	v_readlane_b32 s0, v254, 5
	s_waitcnt lgkmcnt(0)
	s_barrier
	v_readlane_b32 s1, v254, 6
	s_add_u32 s96, s0, 0x4000
	s_getreg_b32 s3, hwreg(HW_REG_XCC_ID, 0, 4)
	s_addc_u32 s97, s1, 0
	s_and_b32 s0, s3, 15
	v_cmp_eq_u32_e64 s[88:89], 0, v0
	s_and_saveexec_b64 s[4:5], s[88:89]
	s_cbranch_execz .LBB0_13
	s_mov_b64 s[6:7], exec
	v_mbcnt_lo_u32_b32 v1, s6, 0
	v_mbcnt_hi_u32_b32 v1, s7, v1
	v_cmp_eq_u32_e32 vcc, 0, v1
	s_and_b64 s[8:9], exec, vcc
	s_mov_b64 exec, s[8:9]
	s_cbranch_execz .LBB0_13
	s_lshl_b32 s3, s0, 8
	s_bcnt1_i32_b64 s6, s[6:7]
	v_mov_b32_e32 v1, s3
	v_mov_b32_e32 v2, s6
	global_atomic_add v1, v2, s[96:97] offset:1024
	s_and_b32 s3, s2, 7
	s_cmp_eq_u32 s3, s0
	s_cbranch_scc1 .Lxmap_ok
	v_mov_b32_e32 v1, 0x100
	v_mov_b32_e32 v2, 1
	global_atomic_add v1, v2, s[96:97]
.Lxmap_ok:
.LBB0_13:
	s_or_b64 exec, exec, s[4:5]
	v_readlane_b32 s1, v254, 0
	s_lshr_b32 s1, s1, 6
	s_cmp_lt_i32 s94, 1
	s_cselect_b64 s[4:5], -1, 0
	s_cmp_gt_i32 s95, 0
	s_cselect_b64 s[6:7], -1, 0
	s_and_b64 s[4:5], s[4:5], s[6:7]
	s_andn2_b64 vcc, exec, s[4:5]
	v_and_b32_e32 v194, 63, v0
	v_writelane_b32 v254, s1, 7
	s_cbranch_vccnz .LBB0_71
	v_readlane_b32 s10, v254, 1
	v_readlane_b32 s11, v254, 2
	s_load_dwordx4 s[4:7], s[10:11], 0x8
	v_lshlrev_b32_e32 v2, 4, v0
	v_mov_b32_e32 v3, 0
	v_add_u32_e32 v1, 0, v2
	s_cmpk_gt_i32 s51, 0xff
	s_waitcnt lgkmcnt(0)
	v_lshl_add_u64 v[16:17], s[4:5], 0, v[2:3]
	v_add_co_u32_e32 v8, vcc, 0x2000, v16
	global_load_dwordx4 v[4:7], v2, s[4:5]
	s_nop 0
	v_addc_co_u32_e32 v9, vcc, 0, v17, vcc
	v_add_co_u32_e32 v12, vcc, 0x4000, v16
	global_load_dwordx4 v[8:11], v[8:9], off
	s_nop 0
	v_addc_co_u32_e32 v13, vcc, 0, v17, vcc
	v_add_co_u32_e32 v16, vcc, 0x6000, v16
	global_load_dwordx4 v[12:15], v[12:13], off
	s_nop 0
	v_addc_co_u32_e32 v17, vcc, 0, v17, vcc
	global_load_dwordx4 v[16:19], v[16:17], off
	s_mov_b32 s5, 0
	s_waitcnt vmcnt(3)
	v_mul_f32_e32 v2, 0xbfb8aa3b, v4
	v_mul_f32_e32 v20, 0xbfb8aa3b, v5
	v_mul_f32_e32 v21, 0xbfb8aa3b, v6
	v_mul_f32_e32 v22, 0xbfb8aa3b, v7
	v_exp_f32_e32 v2, v2
	v_exp_f32_e32 v20, v20
	v_exp_f32_e32 v21, v21
	v_exp_f32_e32 v22, v22
	s_waitcnt vmcnt(2)
	v_mul_f32_e32 v23, 0xbfb8aa3b, v8
	v_mul_f32_e32 v24, 0xbfb8aa3b, v9
	v_mul_f32_e32 v25, 0xbfb8aa3b, v10
	v_mul_f32_e32 v26, 0xbfb8aa3b, v11
	v_exp_f32_e32 v27, v23
	v_exp_f32_e32 v24, v24
	v_exp_f32_e32 v25, v25
	v_exp_f32_e32 v26, v26
	s_waitcnt vmcnt(1)
	v_mul_f32_e32 v23, 0xbfb8aa3b, v12
	v_mul_f32_e32 v28, 0xbfb8aa3b, v13
	v_mul_f32_e32 v29, 0xbfb8aa3b, v14
	v_mul_f32_e32 v30, 0xbfb8aa3b, v15
	v_add_f32_e32 v2, 1.0, v2
	v_add_f32_e32 v31, 1.0, v20
	v_add_f32_e32 v32, 1.0, v21
	v_add_f32_e32 v33, 1.0, v22
	v_exp_f32_e32 v34, v23
	v_exp_f32_e32 v28, v28
	v_exp_f32_e32 v29, v29
	v_exp_f32_e32 v30, v30
	s_waitcnt vmcnt(0)
	v_mul_f32_e32 v35, 0xbfb8aa3b, v16
	v_mul_f32_e32 v36, 0xbfb8aa3b, v17
	v_mul_f32_e32 v37, 0xbfb8aa3b, v18
	v_mul_f32_e32 v38, 0xbfb8aa3b, v19
	v_rcp_f32_e32 v20, v2
	v_rcp_f32_e32 v21, v31
	v_rcp_f32_e32 v22, v32
	v_rcp_f32_e32 v23, v33
	v_exp_f32_e32 v2, v35
	v_exp_f32_e32 v31, v36
	v_exp_f32_e32 v32, v37
	v_exp_f32_e32 v33, v38
	v_add_f32_e32 v27, 1.0, v27
	v_add_f32_e32 v35, 1.0, v24
	v_add_f32_e32 v36, 1.0, v25
	v_add_f32_e32 v37, 1.0, v26
	v_rcp_f32_e32 v24, v27
	v_rcp_f32_e32 v25, v35
	v_rcp_f32_e32 v26, v36
	v_rcp_f32_e32 v27, v37
	v_add_f32_e32 v34, 1.0, v34
	v_add_f32_e32 v28, 1.0, v28
	v_add_f32_e32 v29, 1.0, v29
	v_add_f32_e32 v30, 1.0, v30
	v_pk_mul_f32 v[6:7], v[6:7], v[22:23]
	v_pk_mul_f32 v[4:5], v[4:5], v[20:21]
	v_rcp_f32_e32 v20, v34
	v_rcp_f32_e32 v21, v28
	v_rcp_f32_e32 v22, v29
	v_rcp_f32_e32 v23, v30
	v_add_f32_e32 v2, 1.0, v2
	v_add_f32_e32 v29, 1.0, v31
	v_add_f32_e32 v30, 1.0, v32
	v_add_f32_e32 v31, 1.0, v33
	v_rcp_f32_e32 v28, v2
	v_rcp_f32_e32 v29, v29
	v_rcp_f32_e32 v30, v30
	v_rcp_f32_e32 v31, v31
	ds_write_b128 v1, v[4:7]
	v_pk_mul_f32 v[6:7], v[10:11], v[26:27]
	v_pk_mul_f32 v[4:5], v[8:9], v[24:25]
	ds_write_b128 v1, v[4:7] offset:8192
	v_pk_mul_f32 v[6:7], v[14:15], v[22:23]
	v_pk_mul_f32 v[4:5], v[12:13], v[20:21]
	ds_write_b128 v1, v[4:7] offset:16384
	v_pk_mul_f32 v[6:7], v[18:19], v[30:31]
	v_pk_mul_f32 v[4:5], v[16:17], v[28:29]
	ds_write_b128 v1, v[4:7] offset:24576
	s_waitcnt lgkmcnt(0)
	s_barrier
	s_cbranch_scc1 .LBB0_17
	s_load_dwordx2 s[8:9], s[10:11], 0xd8
	s_load_dwordx2 s[12:13], s[10:11], 0xf8
	v_readlane_b32 s1, v254, 0
	s_and_b32 s3, s1, 0xffffffc0
	v_readlane_b32 s1, v254, 7
	v_mov_b32_e32 v2, 2
	s_lshl_b32 s4, s1, 12
	v_lshlrev_b32_sdwa v2, v2, v0 dst_sel:DWORD dst_unused:UNUSED_PAD src0_sel:DWORD src1_sel:BYTE_0
	s_add_i32 s4, s4, 0
	v_lshlrev_b32_e32 v1, 4, v194
	v_add_u32_e32 v4, 0, v2
	s_waitcnt lgkmcnt(0)
	v_lshl_add_u64 v[2:3], s[12:13], 0, v[2:3]
	s_mov_b64 s[10:11], 0x5da00000
	v_add_u32_e32 v152, s4, v1
	v_lshl_add_u64 v[146:147], v[2:3], 0, s[10:11]
	v_and_b32_e32 v2, 0x100, v0
	s_movk_i32 s4, 0x300
	v_mov_b32_e32 v3, 0x200
	v_lshl_add_u32 v153, v2, 2, v4
	v_or_b32_e32 v2, 0x200, v0
	v_bitop3_b32 v3, v0, s4, v3 bitop3:0xc8
	v_lshrrev_b32_e32 v154, 8, v0
	v_lshl_add_u32 v155, v3, 2, v4
	v_lshrrev_b32_e32 v156, 8, v2
	s_lshl_b32 s26, s51, 8
	s_lshl_b32 s27, s50, 8
	s_movk_i32 s28, 0x1000
	v_mov_b32_e32 v157, 0x3000
	s_mov_b32 s29, s51

; #define PROBE_BEGIN(k) do { if (PROBE_PH == (k)) { __syncthreads(); pr_t0 = __builtin_amdgcn_s_memrealtime(); } } while (0)
; __global__ void __launch_bounds__(NWAVES * 64, 2) fwd_kernel(Args args) {
;     ...
;     if (IN(1)) for (int rep_ = 0; rep_ < REP(1); ++rep_) {
;         PH_PTRS(); PROBE_BEGIN(1);
;         for (int o = vcu * 512 + tid; o < 4 * 8 * D; o += G * 512) { const int b = o >> 14, c = o & (8 * D - 1);
;             const float sacc = (c < 6 * D ? ada_b[c] : fada_b[c - 6 * D]) + MODP[(size_t)(0 * 4 + b) * (8 * D) + c] + MODP[(size_t)(1 * 4 + b) * (8 * D) + c] + MODP[(size_t)(2 * 4 + b) * (8 * D) + c] + MODP[(size_t)(3 * 4 + b) * (8 * D) + c];
;             if (c < 6 * D) MOD[(size_t)b * 6 * D + c] = sacc; else FMOD[(size_t)b * 2 * D + c - 6 * D] = sacc; }
.LBB0_71:
	s_lshl_b32 s3, s51, 3
	v_readlane_b32 s1, v254, 7
	s_add_i32 s1, s3, s1
	s_nop 0
	v_writelane_b32 v254, s1, 8
	s_lshl_b32 s1, s50, 3
	s_cmp_lt_i32 s94, 2
	s_cselect_b64 s[4:5], -1, 0
	s_cmp_gt_i32 s95, 1
	s_cselect_b64 s[6:7], -1, 0
	s_and_b64 s[4:5], s[4:5], s[6:7]
	s_andn2_b64 vcc, exec, s[4:5]
	v_writelane_b32 v254, s1, 9
	s_cbranch_vccnz .LBB0_431
	v_readlane_b32 s6, v254, 1
	v_readlane_b32 s7, v254, 2
	s_load_dwordx2 s[68:69], s[6:7], 0x0
	s_load_dwordx8 s[36:43], s[6:7], 0x18
	s_load_dwordx16 s[16:31], s[6:7], 0x40
	s_load_dwordx4 s[44:47], s[6:7], 0x80
	s_load_dwordx2 s[4:5], s[6:7], 0x98
	s_load_dword s98, s[96:97], 0x100
	v_lshl_or_b32 v1, s51, 9, v0
	s_mov_b32 s3, 0x10000
	v_cmp_gt_i32_e32 vcc, s3, v1
	s_waitcnt lgkmcnt(0)
	v_writelane_b32 v254, s98, 40
	s_nop 1
	v_writelane_b32 v254, s4, 10
	s_nop 1
	v_writelane_b32 v254, s5, 11
	s_load_dwordx2 s[56:57], s[6:7], 0xf8
	s_load_dwordx2 s[4:5], s[6:7], 0xb8
	s_waitcnt lgkmcnt(0)
	s_add_u32 s66, s56, 0x5da00000
	v_writelane_b32 v254, s4, 12
	s_addc_u32 s67, s57, 0
	s_nop 0
	v_writelane_b32 v254, s5, 13
	s_load_dwordx2 s[4:5], s[6:7], 0xc8
	s_waitcnt lgkmcnt(0)
	v_writelane_b32 v254, s4, 14
	s_nop 1
	v_writelane_b32 v254, s5, 15
	s_and_saveexec_b64 s[4:5], vcc
	s_cbranch_execz .LBB0_79
	s_lshl_b32 s3, s50, 9
	s_load_dwordx2 s[6:7], s[6:7], 0xe0
	s_add_u32 s8, s56, 0x100000
	s_addc_u32 s9, s57, 0
	s_add_u32 s10, s56, 0x124000
	s_mov_b32 s14, 0xffff4000
	s_addc_u32 s11, s57, 0
	s_mov_b64 s[12:13], 0
	s_movk_i32 s33, 0x2fff
	s_movk_i32 s48, 0x3000
	v_mov_b32_e32 v3, 0
	s_mov_b32 s15, -1
	s_mov_b32 s49, 0xffff
	s_branch .LBB0_75

; __device__ __forceinline__ unsigned xb_ld(unsigned* p)              { return __hip_atomic_load(p, __ATOMIC_RELAXED, __HIP_MEMORY_SCOPE_AGENT); }
; __device__ __forceinline__ unsigned xb_add(unsigned* p, unsigned v) { return __hip_atomic_fetch_add(p, v, __ATOMIC_RELAXED, __HIP_MEMORY_SCOPE_AGENT); }
; #define XB_SPIN(cond, bar) do { unsigned _sp = 0; while (cond) { __builtin_amdgcn_s_sleep(1); \
;     if ((++_sp & 255u) == 0u) { if (xb_ld(&(bar)[XB_TMO])) break; if (_sp > XB_SPIN_CAP) { atomicAdd(&(bar)[XB_TMO], 1u); break; } } } } while (0)
; __device__ __forceinline__ void xcd_barrier(const XcdBarrier& b) {
;     ...
;         const unsigned old = xb_add(&bar[XB_XSUB(b.x)], 1u);
;         const unsigned gen = old / nloc;
;         if (old + 1u == (gen + 1u) * nloc) {
;             __builtin_amdgcn_fence(__ATOMIC_RELEASE, "agent");
;             asm volatile("s_waitcnt vmcnt(0)" ::: "memory");
;             const unsigned og = xb_add(&bar[XB_TOP], 1u);
;             const unsigned tg = og / nx;
;             if (og + 1u == (tg + 1u) * nx) xb_add(&bar[XB_TOPGEN], 1u);
;             else XB_SPIN(xb_ld(&bar[XB_TOPGEN]) == tg, bar);
;             __builtin_amdgcn_fence(__ATOMIC_ACQUIRE, "agent");
;             xb_add(&bar[XB_XGEN(b.x)], 1u);
;             asm volatile("s_waitcnt vmcnt(0)" ::: "memory");
.LBB0_943:
	s_andn2_saveexec_b64 s[8:9], s[8:9]
	s_cbranch_execz .LBB0_963
	s_mov_b64 s[8:9], exec
	v_readlane_b32 s98, v254, 40
	s_cmp_lg_u32 s98, 0
	s_cbranch_scc1 .Lb7_global
	s_cmpk_eq_i32 s50, 0x100
	s_cbranch_scc1 .LBB0_960
.Lb7_global:
	buffer_wbl2 sc1
	s_waitcnt lgkmcnt(0)
	s_waitcnt vmcnt(0)
	v_mbcnt_lo_u32_b32 v2, s8, 0
	v_mbcnt_hi_u32_b32 v2, s9, v2
	v_cmp_eq_u32_e32 vcc, 0, v2
	s_and_saveexec_b64 s[10:11], vcc
	s_cbranch_execz .LBB0_946
	s_bcnt1_i32_b64 s3, s[8:9]
	v_readlane_b32 s8, v254, 5
	v_mov_b32_e32 v3, 0x7000
	v_mov_b32_e32 v4, s3
	v_readlane_b32 s9, v254, 6
	s_nop 4
	global_atomic_add v3, v3, v4, s[8:9] offset:1024 sc0

; __device__ __forceinline__ unsigned xb_ld(unsigned* p)              { return __hip_atomic_load(p, __ATOMIC_RELAXED, __HIP_MEMORY_SCOPE_AGENT); }
; __device__ __forceinline__ unsigned xb_add(unsigned* p, unsigned v) { return __hip_atomic_fetch_add(p, v, __ATOMIC_RELAXED, __HIP_MEMORY_SCOPE_AGENT); }
; #define XB_SPIN(cond, bar) do { unsigned _sp = 0; while (cond) { __builtin_amdgcn_s_sleep(1); \
;     if ((++_sp & 255u) == 0u) { if (xb_ld(&(bar)[XB_TMO])) break; if (_sp > XB_SPIN_CAP) { atomicAdd(&(bar)[XB_TMO], 1u); break; } } } } while (0)
; __device__ __forceinline__ void xcd_barrier(const XcdBarrier& b) {
;     ...
;         const unsigned old = xb_add(&bar[XB_XSUB(b.x)], 1u);
;         const unsigned gen = old / nloc;
;         if (old + 1u == (gen + 1u) * nloc) {
;             __builtin_amdgcn_fence(__ATOMIC_RELEASE, "agent");
;             asm volatile("s_waitcnt vmcnt(0)" ::: "memory");
;             const unsigned og = xb_add(&bar[XB_TOP], 1u);
;             const unsigned tg = og / nx;
;             if (og + 1u == (tg + 1u) * nx) xb_add(&bar[XB_TOPGEN], 1u);
;             else XB_SPIN(xb_ld(&bar[XB_TOPGEN]) == tg, bar);
;             __builtin_amdgcn_fence(__ATOMIC_ACQUIRE, "agent");
;             xb_add(&bar[XB_XGEN(b.x)], 1u);
;             asm volatile("s_waitcnt vmcnt(0)" ::: "memory");
.LBB0_1032:
	s_andn2_saveexec_b64 s[6:7], s[6:7]
	s_cbranch_execz .LBB0_1052
	s_mov_b64 s[6:7], exec
	v_readlane_b32 s98, v254, 40
	s_cmp_lg_u32 s98, 0
	s_cbranch_scc1 .Lb8_global
	s_cmpk_eq_i32 s50, 0x100
	s_cbranch_scc1 .LBB0_1049
.Lb8_global:
	buffer_wbl2 sc1
	s_waitcnt lgkmcnt(0)
	s_waitcnt vmcnt(0)
	v_mbcnt_lo_u32_b32 v2, s6, 0
	v_mbcnt_hi_u32_b32 v2, s7, v2
	v_cmp_eq_u32_e32 vcc, 0, v2
	s_and_saveexec_b64 s[8:9], vcc
	s_cbranch_execz .LBB0_1035
	s_bcnt1_i32_b64 s6, s[6:7]
	v_mov_b32_e32 v4, s6
	v_readlane_b32 s6, v254, 5
	v_mov_b32_e32 v3, 0x7000
	v_readlane_b32 s7, v254, 6
	s_nop 4
	global_atomic_add v3, v3, v4, s[6:7] offset:1024 sc0
